# MLA step schedule: 3 of the C0 exps moved in front of PV1 (ea=3, e0=5,5,3) to even out the VALU gaps
# baseline (speedup 1.0000x reference)
; #define LAS __attribute__((address_space(3)))
; DEV float ex2(float x) { return __builtin_amdgcn_exp2f(x); }
; #define MLA_SB() __builtin_amdgcn_sched_barrier(0)
; #define MLA_PIN(x) asm volatile("" : "+v"(x))
; #define MFMA8(a, b, c) __builtin_amdgcn_mfma_scale_f32_32x32x64_f8f6f4((a), (b), (c), 0, 0, 0, 0x7f7f7f7f, 0, 0x7c7c7c7c)
; #define MFMA8PV(a, b, c) __builtin_amdgcn_mfma_scale_f32_32x32x64_f8f6f4((a), (b), (c), 0, 1, 0, 0x7f7f7f7f, 0, 0x7f7f7f7f)
; DEV unsigned pk_bf8x4(float a, float b, float c, float d, int old = 0) { int w = __builtin_amdgcn_cvt_pk_bf8_f32(a, b, old, false); w = __builtin_amdgcn_cvt_pk_bf8_f32(c, d, w, true); return (unsigned)w; }
; template <int VAR> DEV void mla_step(f32x16& C0, f32x16& C1, f32x16& P0, f32x16& P1, f32x16& o0, f32x16& o1, f32x16& lacc,
;                   const v8i (&qf)[2], const f32x16& cini, LAS char* kp, LAS char* vp, v8i& pw) {
;     v8i kf[2], vf[2];
;     const v8i ones8 = {0x38383838, 0x38383838, 0x38383838, 0x38383838, 0x38383838, 0x38383838, 0x38383838, 0x38383838};
;     kf[0] = mla_kf8(kp, 0, 0); kf[1] = mla_kf8(kp, 1, 0);
;     MLA_SB();
; #pragma unroll
;     for (int g = 0; g < 4; ++g) {
;         const int kb = g & 1, sx = g >> 1;
;         if (kb) C1 = MFMA8(kf[1], qf[sx], sx == 0 ? cini : C1); else C0 = MFMA8(kf[0], qf[sx], sx == 0 ? cini : C0);
;         if (g < 2) kf[kb] = mla_kf8(kp, kb, 1);
;         if (g >= 2) vf[g - 2] = mla_vf8(vp, g - 2);
; #pragma unroll
;         for (int j = 0; j < 2; ++j) { const int w = 2 * g + j, e = 4 * w;
;             if (VAR == 3) pw[w] = __builtin_bit_cast(int, (e < 16) ? P0[e] : P1[e - 16]);
;             else pw[w] = (int)((e < 16) ? pk_bf8x4(P0[e], P0[e + 1], P0[e + 2], P0[e + 3], pw[w]) : pk_bf8x4(P1[e - 16], P1[e - 15], P1[e - 14], P1[e - 13], pw[w])); }
;         if (g == 3) MLA_PIN(pw);
;         MLA_SB();
;     }
; #pragma unroll
;     for (int g = 0; g < 3; ++g) {
;         if (g == 0) o0 = MFMA8PV(vf[0], pw, o0); else if (g == 1) o1 = MFMA8PV(vf[1], pw, o1); else lacc = MFMA8PV(ones8, pw, lacc);
;         const int e0 = (g * 32) / 3, e1 = ((g + 1) * 32) / 3;
; #pragma unroll
;         for (int e = e0; e < e1; ++e) { if (VAR == 2 || VAR == 3) continue; if (e < 16) C0[e] = ex2(C0[e]); else C1[e - 16] = ex2(C1[e - 16]); }
;         if (g < 2) MLA_PIN(C0);
;         if (g > 0) MLA_PIN(C1);
;         MLA_SB();
;     }
; }
.LBB0_812:
	s_mul_i32 s2, s62, 0x6000
	v_add_u32_e32 v172, s2, v200
	s_add_i32 s3, s62, 1
	s_and_b32 s3, s3, 3
	s_mul_i32 s3, s3, 0x6000
	ds_read_b128 v[98:101], v172 offset:8192
	ds_read_b128 v[106:109], v172 offset:8704
	ds_read_b128 v[102:105], v172 offset:9216
	ds_read_b128 v[110:113], v172 offset:9728
	v_cvt_pk_bf8_f32 v146, v82, v83
	v_cvt_pk_bf8_f32 v147, v86, v87
	v_exp_f32_e32 v69, v69
	v_exp_f32_e32 v70, v70
	v_exp_f32_e32 v71, v71
	s_waitcnt lgkmcnt(1)
	v_mfma_scale_f32_32x32x64_f8f6f4 v[114:129], v[98:105], v[138:145], v[2:17], v209, v208 op_sel_hi:[0,0,0]
	ds_read_b128 v[154:157], v172 offset:12288
	ds_read_b128 v[158:161], v172 offset:13312
	v_cvt_pk_bf8_f32 v146, v84, v85 op_sel:[0,0,1]
	v_cvt_pk_bf8_f32 v147, v88, v89 op_sel:[0,0,1]
	v_cvt_pk_bf8_f32 v148, v90, v91
	v_cvt_pk_bf8_f32 v149, v94, v95
	ds_read_b128 v[82:85], v172 offset:12800
	ds_read_b128 v[86:89], v172 offset:13824
	v_exp_f32_e32 v72, v72
	v_exp_f32_e32 v73, v73
	s_waitcnt lgkmcnt(4)
	v_mfma_scale_f32_32x32x64_f8f6f4 v[98:113], v[106:113], v[138:145], v[2:17], v209, v208 op_sel_hi:[0,0,0]
	v_cvt_pk_bf8_f32 v148, v92, v93 op_sel:[0,0,1]
	v_cvt_pk_bf8_f32 v149, v96, v97 op_sel:[0,0,1]
	ds_read_b128 v[90:93], v172 offset:16384
	ds_read_b128 v[94:97], v172 offset:17408
	v_exp_f32_e32 v74, v74
	v_exp_f32_e32 v75, v75
	v_exp_f32_e32 v76, v76
	s_waitcnt lgkmcnt(4)
	v_mfma_scale_f32_32x32x64_f8f6f4 v[114:129], v[154:161], v[130:137], v[114:129], v209, v208 op_sel_hi:[0,0,0]
	v_exp_f32_e32 v77, v77
	v_exp_f32_e32 v78, v78
	v_exp_f32_e32 v79, v79
	v_exp_f32_e32 v80, v80
	v_exp_f32_e32 v81, v81
	s_waitcnt lgkmcnt(2)
	v_mfma_scale_f32_32x32x64_f8f6f4 v[98:113], v[82:89], v[130:137], v[98:113], v209, v208 op_sel_hi:[0,0,0]
	v_cvt_pk_bf8_f32 v150, v66, v67
	v_cvt_pk_bf8_f32 v151, v70, v71
	v_cvt_pk_bf8_f32 v150, v68, v69 op_sel:[0,0,1]
	v_cvt_pk_bf8_f32 v151, v72, v73 op_sel:[0,0,1]
	v_cvt_pk_bf8_f32 v152, v74, v75
	v_cvt_pk_bf8_f32 v153, v78, v79
	v_cvt_pk_bf8_f32 v152, v76, v77 op_sel:[0,0,1]
	v_cvt_pk_bf8_f32 v153, v80, v81 op_sel:[0,0,1]
	ds_read_b128 v[66:69], v172 offset:16896
	ds_read_b128 v[70:73], v172 offset:17920
	s_nop 2
	v_exp_f32_e32 v114, v114
	v_exp_f32_e32 v115, v115
	v_exp_f32_e32 v116, v116
	s_waitcnt lgkmcnt(2)
	v_mfma_scale_f32_32x32x64_f8f6f4 v[50:65], v[90:97], v[146:153], v[50:65], v209, v209 op_sel_hi:[0,0,0] blgp:1
	v_exp_f32_e32 v117, v117
	v_exp_f32_e32 v118, v118
	v_exp_f32_e32 v119, v119
	v_exp_f32_e32 v120, v120
	v_exp_f32_e32 v121, v121
	v_add_u32_e32 v173, s3, v200
	ds_read_b128 v[74:77], v173 offset:512
	ds_read_b128 v[78:81], v173 offset:1536
	s_waitcnt lgkmcnt(2)
	v_mfma_scale_f32_32x32x64_f8f6f4 v[18:33], v[66:73], v[146:153], v[18:33], v209, v209 op_sel_hi:[0,0,0] blgp:1
	v_exp_f32_e32 v122, v122
	v_exp_f32_e32 v123, v123
	v_exp_f32_e32 v124, v124
	v_exp_f32_e32 v125, v125
	v_exp_f32_e32 v126, v126
	ds_read_b128 v[66:69], v173
	ds_read_b128 v[70:73], v173 offset:1024
	v_mfma_scale_f32_32x32x64_f8f6f4 v[34:49], v[210:217], v[146:153], v[34:49], v209, v209 op_sel_hi:[0,0,0] blgp:1
	v_exp_f32_e32 v127, v127
	v_exp_f32_e32 v128, v128
	v_exp_f32_e32 v129, v129
	v_exp_f32_e32 v98, v98
	v_exp_f32_e32 v99, v99
	v_exp_f32_e32 v100, v100
	s_add_i32 s61, s61, 1
	s_add_i32 s2, s62, 1
	s_and_b32 s62, s2, 3
	s_mul_i32 s64, s62, 0x6000
	s_add_i32 s2, s62, 2
	s_and_b32 s2, s2, 3
	s_mul_i32 s2, s2, 0x6000
	s_cmp_eq_u32 s62, 2
	s_cselect_b64 s[8:9], -1, 0
	s_cmp_eq_u32 s100, 0
	s_cbranch_scc1 .Lmla_w0
	s_cmp_eq_u32 s100, 1
	s_cbranch_scc1 .Lmla_w1
	s_waitcnt vmcnt(2)
	s_branch .Lmla_wd

; #define LAS __attribute__((address_space(3)))
; DEV float ex2(float x) { return __builtin_amdgcn_exp2f(x); }
; #define MLA_SB() __builtin_amdgcn_sched_barrier(0)
; #define MLA_PIN(x) asm volatile("" : "+v"(x))
; #define MFMA8(a, b, c) __builtin_amdgcn_mfma_scale_f32_32x32x64_f8f6f4((a), (b), (c), 0, 0, 0, 0x7f7f7f7f, 0, 0x7c7c7c7c)
; #define MFMA8PV(a, b, c) __builtin_amdgcn_mfma_scale_f32_32x32x64_f8f6f4((a), (b), (c), 0, 1, 0, 0x7f7f7f7f, 0, 0x7f7f7f7f)
; DEV unsigned pk_bf8x4(float a, float b, float c, float d, int old = 0) { int w = __builtin_amdgcn_cvt_pk_bf8_f32(a, b, old, false); w = __builtin_amdgcn_cvt_pk_bf8_f32(c, d, w, true); return (unsigned)w; }
; template <int VAR> DEV void mla_step(f32x16& C0, f32x16& C1, f32x16& P0, f32x16& P1, f32x16& o0, f32x16& o1, f32x16& lacc,
;                   const v8i (&qf)[2], const f32x16& cini, LAS char* kp, LAS char* vp, v8i& pw) {
;     v8i kf[2], vf[2];
;     const v8i ones8 = {0x38383838, 0x38383838, 0x38383838, 0x38383838, 0x38383838, 0x38383838, 0x38383838, 0x38383838};
;     kf[0] = mla_kf8(kp, 0, 0); kf[1] = mla_kf8(kp, 1, 0);
;     MLA_SB();
; #pragma unroll
;     for (int g = 0; g < 4; ++g) {
;         const int kb = g & 1, sx = g >> 1;
;         if (kb) C1 = MFMA8(kf[1], qf[sx], sx == 0 ? cini : C1); else C0 = MFMA8(kf[0], qf[sx], sx == 0 ? cini : C0);
;         if (g < 2) kf[kb] = mla_kf8(kp, kb, 1);
;         if (g >= 2) vf[g - 2] = mla_vf8(vp, g - 2);
; #pragma unroll
;         for (int j = 0; j < 2; ++j) { const int w = 2 * g + j, e = 4 * w;
;             if (VAR == 3) pw[w] = __builtin_bit_cast(int, (e < 16) ? P0[e] : P1[e - 16]);
;             else pw[w] = (int)((e < 16) ? pk_bf8x4(P0[e], P0[e + 1], P0[e + 2], P0[e + 3], pw[w]) : pk_bf8x4(P1[e - 16], P1[e - 15], P1[e - 14], P1[e - 13], pw[w])); }
;         if (g == 3) MLA_PIN(pw);
;         MLA_SB();
;     }
; #pragma unroll
;     for (int g = 0; g < 3; ++g) {
;         if (g == 0) o0 = MFMA8PV(vf[0], pw, o0); else if (g == 1) o1 = MFMA8PV(vf[1], pw, o1); else lacc = MFMA8PV(ones8, pw, lacc);
;         const int e0 = (g * 32) / 3, e1 = ((g + 1) * 32) / 3;
; #pragma unroll
;         for (int e = e0; e < e1; ++e) { if (VAR == 2 || VAR == 3) continue; if (e < 16) C0[e] = ex2(C0[e]); else C1[e - 16] = ex2(C1[e - 16]); }
;         if (g < 2) MLA_PIN(C0);
;         if (g > 0) MLA_PIN(C1);
;         MLA_SB();
;     }
; }
.Lmla_wd:
	s_waitcnt lgkmcnt(0)
	s_barrier
	s_add_i32 s2, s2, s60
	s_mov_b32 s3, m0
	s_mov_b32 m0, s2
	v_cvt_pk_bf8_f32 v146, v114, v115
	v_cvt_pk_bf8_f32 v147, v118, v119
	v_exp_f32_e32 v101, v101
	v_exp_f32_e32 v102, v102
	v_exp_f32_e32 v103, v103
	s_waitcnt lgkmcnt(0)
	v_mfma_scale_f32_32x32x64_f8f6f4 v[82:97], v[66:73], v[138:145], v[2:17], v209, v208 op_sel_hi:[0,0,0]
	global_load_lds_dwordx4 v[162:163], off
	ds_read_b128 v[164:167], v173 offset:4096
	ds_read_b128 v[168:171], v173 offset:5120
	v_cvt_pk_bf8_f32 v146, v116, v117 op_sel:[0,0,1]
	v_cvt_pk_bf8_f32 v147, v120, v121 op_sel:[0,0,1]
	v_cvt_pk_bf8_f32 v148, v122, v123
	v_cvt_pk_bf8_f32 v149, v126, v127
	ds_read_b128 v[114:117], v173 offset:4608
	ds_read_b128 v[118:121], v173 offset:5632
	v_exp_f32_e32 v104, v104
	v_exp_f32_e32 v105, v105
	s_waitcnt lgkmcnt(4)
	v_mfma_scale_f32_32x32x64_f8f6f4 v[66:81], v[74:81], v[138:145], v[2:17], v209, v208 op_sel_hi:[0,0,0]
	global_load_lds_dwordx4 v[162:163], off offset:1024
	v_cvt_pk_bf8_f32 v148, v124, v125 op_sel:[0,0,1]
	v_cvt_pk_bf8_f32 v149, v128, v129 op_sel:[0,0,1]
	ds_read_b128 v[122:125], v172 offset:20480
	ds_read_b128 v[126:129], v172 offset:21504
	v_exp_f32_e32 v106, v106
	v_exp_f32_e32 v107, v107
	v_exp_f32_e32 v108, v108
	s_waitcnt lgkmcnt(4)
	v_mfma_scale_f32_32x32x64_f8f6f4 v[82:97], v[164:171], v[130:137], v[82:97], v209, v208 op_sel_hi:[0,0,0]
	global_load_lds_dwordx4 v[162:163], off offset:2048
	s_mov_b32 m0, s3
	v_exp_f32_e32 v109, v109
	v_exp_f32_e32 v110, v110
	v_exp_f32_e32 v111, v111
	v_exp_f32_e32 v112, v112
	v_exp_f32_e32 v113, v113
	s_waitcnt lgkmcnt(2)
	v_mfma_scale_f32_32x32x64_f8f6f4 v[66:81], v[114:121], v[130:137], v[66:81], v209, v208 op_sel_hi:[0,0,0]
	v_cvt_pk_bf8_f32 v150, v98, v99
	v_cvt_pk_bf8_f32 v151, v102, v103
	v_cvt_pk_bf8_f32 v150, v100, v101 op_sel:[0,0,1]
	v_cvt_pk_bf8_f32 v151, v104, v105 op_sel:[0,0,1]
	v_cvt_pk_bf8_f32 v152, v106, v107
	v_cvt_pk_bf8_f32 v153, v110, v111
	v_cvt_pk_bf8_f32 v152, v108, v109 op_sel:[0,0,1]
	v_cvt_pk_bf8_f32 v153, v112, v113 op_sel:[0,0,1]
	ds_read_b128 v[98:101], v172 offset:20992
	ds_read_b128 v[102:105], v172 offset:22016
	s_nop 2
	v_exp_f32_e32 v82, v82
	v_exp_f32_e32 v83, v83
	v_exp_f32_e32 v84, v84
	s_waitcnt lgkmcnt(2)
	v_mfma_scale_f32_32x32x64_f8f6f4 v[50:65], v[122:129], v[146:153], v[50:65], v209, v209 op_sel_hi:[0,0,0] blgp:1
	v_exp_f32_e32 v85, v85
	v_exp_f32_e32 v86, v86
	v_exp_f32_e32 v87, v87
	v_exp_f32_e32 v88, v88
	v_exp_f32_e32 v89, v89
	s_waitcnt lgkmcnt(0)
	v_mfma_scale_f32_32x32x64_f8f6f4 v[18:33], v[98:105], v[146:153], v[18:33], v209, v209 op_sel_hi:[0,0,0] blgp:1
	v_exp_f32_e32 v90, v90
	v_exp_f32_e32 v91, v91
	v_exp_f32_e32 v92, v92
	v_exp_f32_e32 v93, v93
	v_exp_f32_e32 v94, v94
	v_mfma_scale_f32_32x32x64_f8f6f4 v[34:49], v[210:217], v[146:153], v[34:49], v209, v209 op_sel_hi:[0,0,0] blgp:1
	v_exp_f32_e32 v95, v95
	v_exp_f32_e32 v96, v96
	v_exp_f32_e32 v97, v97
	v_exp_f32_e32 v66, v66
	v_exp_f32_e32 v67, v67
	v_exp_f32_e32 v68, v68
	s_mov_b64 s[20:21], 0x6000
	s_cmpk_lg_i32 s61, 0x80
	v_lshl_add_u64 v[162:163], v[162:163], 0, s[20:21]
	s_cbranch_scc0 .LBB0_835
